# final_phase_4_rows_per_iteration_16B_loads
# baseline (speedup 1.0000x reference)
.LBB0_1110:
	v_readlane_b32 s26, v253, 54
	v_readlane_b32 s27, v253, 55
	v_readlane_b32 s1, v253, 29
	v_readlane_b32 s22, v253, 50
	v_readlane_b32 s23, v253, 51
	v_readlane_b32 s24, v253, 52
	v_readlane_b32 s25, v253, 53
	v_and_b32_e32 v104, 63, v0
	v_lshlrev_b32_e32 v105, 4, v104
	v_lshlrev_b32_e32 v106, 2, v104
	v_lshlrev_b32_e32 v107, 5, v104
	v_mov_b32_e32 v108, 0x358637bd
	v_mov_b32_e32 v109, 0x260
	s_mov_b32 s35, 0xf800000
	s_lshl_b32 s0, s5, 3
	s_add_i32 s2, s0, s1
	s_lshl_b32 s20, s37, 3
	s_mul_i32 s21, s20, 4
	s_add_u32 s4, s26, 0x400000
	s_addc_u32 s5, s27, 0
	s_add_u32 s6, s26, 0x4a000000
	s_addc_u32 s7, s27, 0
	s_add_u32 s8, s26, 0x27000000
	s_addc_u32 s9, s27, 0
	s_cmp_lt_i32 s2, 0x8000
	s_cbranch_scc0 .LBB0_1150
	global_load_dwordx4 v[112:115], v107, s[22:23]
	global_load_dwordx4 v[116:119], v107, s[22:23] offset:16
	global_load_dwordx4 v[120:123], v107, s[22:23] offset:2048
	global_load_dwordx4 v[124:127], v107, s[22:23] offset:2064
	s_mov_b32 s34, s2
	s_lshl_b32 s10, s34, 11
	s_add_u32 s10, s6, s10
	s_addc_u32 s11, s7, 0
	s_lshl_b32 s12, s34, 6
	s_add_u32 s12, s4, s12
	s_addc_u32 s13, s5, 0
	global_load_dwordx4 v[0:3], v105, s[10:11]
	global_load_dwordx4 v[4:7], v105, s[10:11] offset:1024
	global_load_dword v32, v106, s[12:13]
	s_add_i32 s34, s34, s20
	s_cmp_lt_i32 s34, 0x8000
	s_cbranch_scc0 .Lfin_pf_first
	s_lshl_b32 s10, s34, 11
	s_add_u32 s10, s6, s10
	s_addc_u32 s11, s7, 0
	s_lshl_b32 s12, s34, 6
	s_add_u32 s12, s4, s12
	s_addc_u32 s13, s5, 0
	global_load_dwordx4 v[8:11], v105, s[10:11]
	global_load_dwordx4 v[12:15], v105, s[10:11] offset:1024
	global_load_dword v33, v106, s[12:13]
	s_add_i32 s34, s34, s20
	s_cmp_lt_i32 s34, 0x8000
	s_cbranch_scc0 .Lfin_pf_first
	s_lshl_b32 s10, s34, 11
	s_add_u32 s10, s6, s10
	s_addc_u32 s11, s7, 0
	s_lshl_b32 s12, s34, 6
	s_add_u32 s12, s4, s12
	s_addc_u32 s13, s5, 0
	global_load_dwordx4 v[16:19], v105, s[10:11]
	global_load_dwordx4 v[20:23], v105, s[10:11] offset:1024
	global_load_dword v34, v106, s[12:13]
	s_add_i32 s34, s34, s20
	s_cmp_lt_i32 s34, 0x8000
	s_cbranch_scc0 .Lfin_pf_first
	s_lshl_b32 s10, s34, 11
	s_add_u32 s10, s6, s10
	s_addc_u32 s11, s7, 0
	s_lshl_b32 s12, s34, 6
	s_add_u32 s12, s4, s12
	s_addc_u32 s13, s5, 0
	global_load_dwordx4 v[24:27], v105, s[10:11]
	global_load_dwordx4 v[28:31], v105, s[10:11] offset:1024
	global_load_dword v35, v106, s[12:13]

.Lfin_loop:
	s_add_i32 s3, s2, s20
	s_cmp_lt_i32 s3, 0x8000
	s_cselect_b32 s29, 1, 0
	s_add_i32 s43, s3, s20
	s_cmp_lt_i32 s43, 0x8000
	s_cselect_b32 s46, 1, 0
	s_add_i32 s44, s43, s20
	s_cmp_lt_i32 s44, 0x8000
	s_cselect_b32 s47, 1, 0
	s_cmp_lg_u32 s28, 0
	s_cbranch_scc1 .Lfin_nowait
	s_waitcnt vmcnt(0)
.Lfin_nowait:
	v_lshlrev_b32_e32 v40, 16, v0
	v_and_b32_e32 v41, 0xffff0000, v0
	v_lshlrev_b32_e32 v42, 16, v1
	v_and_b32_e32 v43, 0xffff0000, v1
	v_lshlrev_b32_e32 v44, 16, v2
	v_and_b32_e32 v45, 0xffff0000, v2
	v_lshlrev_b32_e32 v46, 16, v3
	v_and_b32_e32 v47, 0xffff0000, v3
	v_lshlrev_b32_e32 v48, 16, v4
	v_and_b32_e32 v49, 0xffff0000, v4
	v_lshlrev_b32_e32 v50, 16, v5
	v_and_b32_e32 v51, 0xffff0000, v5
	v_lshlrev_b32_e32 v52, 16, v6
	v_and_b32_e32 v53, 0xffff0000, v6
	v_lshlrev_b32_e32 v54, 16, v7
	v_and_b32_e32 v55, 0xffff0000, v7
	v_lshlrev_b32_e32 v56, 16, v8
	v_and_b32_e32 v57, 0xffff0000, v8
	v_lshlrev_b32_e32 v58, 16, v9
	v_and_b32_e32 v59, 0xffff0000, v9
	v_lshlrev_b32_e32 v60, 16, v10
	v_and_b32_e32 v61, 0xffff0000, v10
	v_lshlrev_b32_e32 v62, 16, v11
	v_and_b32_e32 v63, 0xffff0000, v11
	v_lshlrev_b32_e32 v64, 16, v12
	v_and_b32_e32 v65, 0xffff0000, v12
	v_lshlrev_b32_e32 v66, 16, v13
	v_and_b32_e32 v67, 0xffff0000, v13
	v_lshlrev_b32_e32 v68, 16, v14
	v_and_b32_e32 v69, 0xffff0000, v14
	v_lshlrev_b32_e32 v70, 16, v15
	v_and_b32_e32 v71, 0xffff0000, v15
	v_lshlrev_b32_e32 v72, 16, v16
	v_and_b32_e32 v73, 0xffff0000, v16
	v_lshlrev_b32_e32 v74, 16, v17
	v_and_b32_e32 v75, 0xffff0000, v17
	v_lshlrev_b32_e32 v76, 16, v18
	v_and_b32_e32 v77, 0xffff0000, v18
	v_lshlrev_b32_e32 v78, 16, v19
	v_and_b32_e32 v79, 0xffff0000, v19
	v_lshlrev_b32_e32 v80, 16, v20
	v_and_b32_e32 v81, 0xffff0000, v20
	v_lshlrev_b32_e32 v82, 16, v21
	v_and_b32_e32 v83, 0xffff0000, v21
	v_lshlrev_b32_e32 v84, 16, v22
	v_and_b32_e32 v85, 0xffff0000, v22
	v_lshlrev_b32_e32 v86, 16, v23
	v_and_b32_e32 v87, 0xffff0000, v23
	v_lshlrev_b32_e32 v88, 16, v24
	v_and_b32_e32 v89, 0xffff0000, v24
	v_lshlrev_b32_e32 v90, 16, v25
	v_and_b32_e32 v91, 0xffff0000, v25
	v_lshlrev_b32_e32 v92, 16, v26
	v_and_b32_e32 v93, 0xffff0000, v26
	v_lshlrev_b32_e32 v94, 16, v27
	v_and_b32_e32 v95, 0xffff0000, v27
	v_lshlrev_b32_e32 v96, 16, v28
	v_and_b32_e32 v97, 0xffff0000, v28
	v_lshlrev_b32_e32 v98, 16, v29
	v_and_b32_e32 v99, 0xffff0000, v29
	v_lshlrev_b32_e32 v100, 16, v30
	v_and_b32_e32 v101, 0xffff0000, v30
	v_lshlrev_b32_e32 v102, 16, v31
	v_and_b32_e32 v103, 0xffff0000, v31
	v_mov_b32_e32 v36, v32
	v_mov_b32_e32 v37, v33
	v_mov_b32_e32 v38, v34
	v_mov_b32_e32 v39, v35
	v_cmp_lt_i32_e32 vcc, -1, v36
	s_and_b32 s30, vcc_lo, 0xffff
	v_cmp_lt_i32_e32 vcc, -1, v37
	s_and_b32 s31, vcc_lo, 0xffff
	s_cmp_eq_u32 s29, 0
	s_cselect_b32 s31, 0, s31
	v_cmp_lt_i32_e32 vcc, -1, v38
	s_and_b32 s40, vcc_lo, 0xffff
	s_cmp_eq_u32 s46, 0
	s_cselect_b32 s40, 0, s40
	v_cmp_lt_i32_e32 vcc, -1, v39
	s_and_b32 s41, vcc_lo, 0xffff
	s_cmp_eq_u32 s47, 0
	s_cselect_b32 s41, 0, s41
	s_add_i32 s33, s2, s21
	s_cmp_lt_i32 s33, 0x8000
	s_cbranch_scc0 .Lfin_pf_next
	s_mov_b32 s34, s33
	s_lshl_b32 s10, s34, 11
	s_add_u32 s10, s6, s10
	s_addc_u32 s11, s7, 0
	s_lshl_b32 s12, s34, 6
	s_add_u32 s12, s4, s12
	s_addc_u32 s13, s5, 0
	global_load_dwordx4 v[0:3], v105, s[10:11]
	global_load_dwordx4 v[4:7], v105, s[10:11] offset:1024
	global_load_dword v32, v106, s[12:13]
	s_add_i32 s34, s34, s20
	s_cmp_lt_i32 s34, 0x8000
	s_cbranch_scc0 .Lfin_pf_next
	s_lshl_b32 s10, s34, 11
	s_add_u32 s10, s6, s10
	s_addc_u32 s11, s7, 0
	s_lshl_b32 s12, s34, 6
	s_add_u32 s12, s4, s12
	s_addc_u32 s13, s5, 0
	global_load_dwordx4 v[8:11], v105, s[10:11]
	global_load_dwordx4 v[12:15], v105, s[10:11] offset:1024
	global_load_dword v33, v106, s[12:13]
	s_add_i32 s34, s34, s20
	s_cmp_lt_i32 s34, 0x8000
	s_cbranch_scc0 .Lfin_pf_next
	s_lshl_b32 s10, s34, 11
	s_add_u32 s10, s6, s10
	s_addc_u32 s11, s7, 0
	s_lshl_b32 s12, s34, 6
	s_add_u32 s12, s4, s12
	s_addc_u32 s13, s5, 0
	global_load_dwordx4 v[16:19], v105, s[10:11]
	global_load_dwordx4 v[20:23], v105, s[10:11] offset:1024
	global_load_dword v34, v106, s[12:13]
	s_add_i32 s34, s34, s20
	s_cmp_lt_i32 s34, 0x8000
	s_cbranch_scc0 .Lfin_pf_next
	s_lshl_b32 s10, s34, 11
	s_add_u32 s10, s6, s10
	s_addc_u32 s11, s7, 0
	s_lshl_b32 s12, s34, 6
	s_add_u32 s12, s4, s12
	s_addc_u32 s13, s5, 0
	global_load_dwordx4 v[24:27], v105, s[10:11]
	global_load_dwordx4 v[28:31], v105, s[10:11] offset:1024
	global_load_dword v35, v106, s[12:13]
.Lfin_pf_next:
	s_mov_b32 s28, 0
	s_or_b32 s0, s30, s31
	s_or_b32 s0, s0, s40
	s_or_b32 s0, s0, s41
	s_cmp_eq_u32 s0, 0
	s_cbranch_scc1 .Lfin_rounds_done
.Lfin_round:
	s_add_i32 s28, s28, 1
	s_mov_b32 s36, 0
	s_cmp_eq_u32 s30, 0
	s_cbranch_scc1 .Lfin_iss_0_done
	s_ff1_i32_b32 s14, s30
	s_bitset0_b32 s30, s14
	v_readlane_b32 s15, v36, s14
	s_lshl_b32 s15, s15, 11
	s_add_u32 s16, s8, s15
	s_addc_u32 s17, s9, 0
	global_load_dwordx4 v[128:131], v105, s[16:17]
	global_load_dwordx4 v[132:135], v105, s[16:17] offset:1024
	s_bitset1_b32 s36, 0
	s_cmp_eq_u32 s30, 0
	s_cbranch_scc1 .Lfin_iss_0_done
	s_ff1_i32_b32 s14, s30
	s_bitset0_b32 s30, s14
	v_readlane_b32 s15, v36, s14
	s_lshl_b32 s15, s15, 11
	s_add_u32 s16, s8, s15
	s_addc_u32 s17, s9, 0
	global_load_dwordx4 v[136:139], v105, s[16:17]
	global_load_dwordx4 v[140:143], v105, s[16:17] offset:1024
	s_bitset1_b32 s36, 1
	s_cmp_eq_u32 s30, 0
	s_cbranch_scc1 .Lfin_iss_0_done
	s_ff1_i32_b32 s14, s30
	s_bitset0_b32 s30, s14
	v_readlane_b32 s15, v36, s14
	s_lshl_b32 s15, s15, 11
	s_add_u32 s16, s8, s15
	s_addc_u32 s17, s9, 0
	global_load_dwordx4 v[144:147], v105, s[16:17]
	global_load_dwordx4 v[148:151], v105, s[16:17] offset:1024
	s_bitset1_b32 s36, 2
.Lfin_iss_0_done:
	s_cmp_eq_u32 s31, 0
	s_cbranch_scc1 .Lfin_iss_1_done
	s_ff1_i32_b32 s14, s31
	s_bitset0_b32 s31, s14
	v_readlane_b32 s15, v37, s14
	s_lshl_b32 s15, s15, 11
	s_add_u32 s16, s8, s15
	s_addc_u32 s17, s9, 0
	global_load_dwordx4 v[152:155], v105, s[16:17]
	global_load_dwordx4 v[156:159], v105, s[16:17] offset:1024
	s_bitset1_b32 s36, 3
	s_cmp_eq_u32 s31, 0
	s_cbranch_scc1 .Lfin_iss_1_done
	s_ff1_i32_b32 s14, s31
	s_bitset0_b32 s31, s14
	v_readlane_b32 s15, v37, s14
	s_lshl_b32 s15, s15, 11
	s_add_u32 s16, s8, s15
	s_addc_u32 s17, s9, 0
	global_load_dwordx4 v[160:163], v105, s[16:17]
	global_load_dwordx4 v[164:167], v105, s[16:17] offset:1024
	s_bitset1_b32 s36, 4
	s_cmp_eq_u32 s31, 0
	s_cbranch_scc1 .Lfin_iss_1_done
	s_ff1_i32_b32 s14, s31
	s_bitset0_b32 s31, s14
	v_readlane_b32 s15, v37, s14
	s_lshl_b32 s15, s15, 11
	s_add_u32 s16, s8, s15
	s_addc_u32 s17, s9, 0
	global_load_dwordx4 v[168:171], v105, s[16:17]
	global_load_dwordx4 v[172:175], v105, s[16:17] offset:1024
	s_bitset1_b32 s36, 5
.Lfin_iss_1_done:
	s_cmp_eq_u32 s40, 0
	s_cbranch_scc1 .Lfin_iss_2_done
	s_ff1_i32_b32 s14, s40
	s_bitset0_b32 s40, s14
	v_readlane_b32 s15, v38, s14
	s_lshl_b32 s15, s15, 11
	s_add_u32 s16, s8, s15
	s_addc_u32 s17, s9, 0
	global_load_dwordx4 v[176:179], v105, s[16:17]
	global_load_dwordx4 v[180:183], v105, s[16:17] offset:1024
	s_bitset1_b32 s36, 6
	s_cmp_eq_u32 s40, 0
	s_cbranch_scc1 .Lfin_iss_2_done
	s_ff1_i32_b32 s14, s40
	s_bitset0_b32 s40, s14
	v_readlane_b32 s15, v38, s14
	s_lshl_b32 s15, s15, 11
	s_add_u32 s16, s8, s15
	s_addc_u32 s17, s9, 0
	global_load_dwordx4 v[184:187], v105, s[16:17]
	global_load_dwordx4 v[188:191], v105, s[16:17] offset:1024
	s_bitset1_b32 s36, 7
	s_cmp_eq_u32 s40, 0
	s_cbranch_scc1 .Lfin_iss_2_done
	s_ff1_i32_b32 s14, s40
	s_bitset0_b32 s40, s14
	v_readlane_b32 s15, v38, s14
	s_lshl_b32 s15, s15, 11
	s_add_u32 s16, s8, s15
	s_addc_u32 s17, s9, 0
	global_load_dwordx4 v[192:195], v105, s[16:17]
	global_load_dwordx4 v[196:199], v105, s[16:17] offset:1024
	s_bitset1_b32 s36, 8
.Lfin_iss_2_done:
	s_cmp_eq_u32 s41, 0
	s_cbranch_scc1 .Lfin_iss_3_done
	s_ff1_i32_b32 s14, s41
	s_bitset0_b32 s41, s14
	v_readlane_b32 s15, v39, s14
	s_lshl_b32 s15, s15, 11
	s_add_u32 s16, s8, s15
	s_addc_u32 s17, s9, 0
	global_load_dwordx4 v[200:203], v105, s[16:17]
	global_load_dwordx4 v[204:207], v105, s[16:17] offset:1024
	s_bitset1_b32 s36, 9
	s_cmp_eq_u32 s41, 0
	s_cbranch_scc1 .Lfin_iss_3_done
	s_ff1_i32_b32 s14, s41
	s_bitset0_b32 s41, s14
	v_readlane_b32 s15, v39, s14
	s_lshl_b32 s15, s15, 11
	s_add_u32 s16, s8, s15
	s_addc_u32 s17, s9, 0
	global_load_dwordx4 v[208:211], v105, s[16:17]
	global_load_dwordx4 v[212:215], v105, s[16:17] offset:1024
	s_bitset1_b32 s36, 10
	s_cmp_eq_u32 s41, 0
	s_cbranch_scc1 .Lfin_iss_3_done
	s_ff1_i32_b32 s14, s41
	s_bitset0_b32 s41, s14
	v_readlane_b32 s15, v39, s14
	s_lshl_b32 s15, s15, 11
	s_add_u32 s16, s8, s15
	s_addc_u32 s17, s9, 0
	global_load_dwordx4 v[216:219], v105, s[16:17]
	global_load_dwordx4 v[220:223], v105, s[16:17] offset:1024
	s_bitset1_b32 s36, 11
.Lfin_iss_3_done:
	s_waitcnt vmcnt(0)
	s_bitcmp1_b32 s36, 0
	s_cbranch_scc0 .Lfin_add_skip_0
	v_lshlrev_b32_e32 v224, 16, v128
	v_and_b32_e32 v225, 0xffff0000, v128
	v_pk_add_f32 v[40:41], v[40:41], v[224:225]
	v_lshlrev_b32_e32 v226, 16, v129
	v_and_b32_e32 v227, 0xffff0000, v129
	v_pk_add_f32 v[42:43], v[42:43], v[226:227]
	v_lshlrev_b32_e32 v228, 16, v130
	v_and_b32_e32 v229, 0xffff0000, v130
	v_pk_add_f32 v[44:45], v[44:45], v[228:229]
	v_lshlrev_b32_e32 v230, 16, v131
	v_and_b32_e32 v231, 0xffff0000, v131
	v_pk_add_f32 v[46:47], v[46:47], v[230:231]
	v_lshlrev_b32_e32 v232, 16, v132
	v_and_b32_e32 v233, 0xffff0000, v132
	v_pk_add_f32 v[48:49], v[48:49], v[232:233]
	v_lshlrev_b32_e32 v234, 16, v133
	v_and_b32_e32 v235, 0xffff0000, v133
	v_pk_add_f32 v[50:51], v[50:51], v[234:235]
	v_lshlrev_b32_e32 v236, 16, v134
	v_and_b32_e32 v237, 0xffff0000, v134
	v_pk_add_f32 v[52:53], v[52:53], v[236:237]
	v_lshlrev_b32_e32 v238, 16, v135
	v_and_b32_e32 v239, 0xffff0000, v135
	v_pk_add_f32 v[54:55], v[54:55], v[238:239]
.Lfin_add_skip_0:
	s_bitcmp1_b32 s36, 1
	s_cbranch_scc0 .Lfin_add_skip_1
	v_lshlrev_b32_e32 v224, 16, v136
	v_and_b32_e32 v225, 0xffff0000, v136
	v_pk_add_f32 v[40:41], v[40:41], v[224:225]
	v_lshlrev_b32_e32 v226, 16, v137
	v_and_b32_e32 v227, 0xffff0000, v137
	v_pk_add_f32 v[42:43], v[42:43], v[226:227]
	v_lshlrev_b32_e32 v228, 16, v138
	v_and_b32_e32 v229, 0xffff0000, v138
	v_pk_add_f32 v[44:45], v[44:45], v[228:229]
	v_lshlrev_b32_e32 v230, 16, v139
	v_and_b32_e32 v231, 0xffff0000, v139
	v_pk_add_f32 v[46:47], v[46:47], v[230:231]
	v_lshlrev_b32_e32 v232, 16, v140
	v_and_b32_e32 v233, 0xffff0000, v140
	v_pk_add_f32 v[48:49], v[48:49], v[232:233]
	v_lshlrev_b32_e32 v234, 16, v141
	v_and_b32_e32 v235, 0xffff0000, v141
	v_pk_add_f32 v[50:51], v[50:51], v[234:235]
	v_lshlrev_b32_e32 v236, 16, v142
	v_and_b32_e32 v237, 0xffff0000, v142
	v_pk_add_f32 v[52:53], v[52:53], v[236:237]
	v_lshlrev_b32_e32 v238, 16, v143
	v_and_b32_e32 v239, 0xffff0000, v143
	v_pk_add_f32 v[54:55], v[54:55], v[238:239]
.Lfin_add_skip_1:
	s_bitcmp1_b32 s36, 2
	s_cbranch_scc0 .Lfin_add_skip_2
	v_lshlrev_b32_e32 v224, 16, v144
	v_and_b32_e32 v225, 0xffff0000, v144
	v_pk_add_f32 v[40:41], v[40:41], v[224:225]
	v_lshlrev_b32_e32 v226, 16, v145
	v_and_b32_e32 v227, 0xffff0000, v145
	v_pk_add_f32 v[42:43], v[42:43], v[226:227]
	v_lshlrev_b32_e32 v228, 16, v146
	v_and_b32_e32 v229, 0xffff0000, v146
	v_pk_add_f32 v[44:45], v[44:45], v[228:229]
	v_lshlrev_b32_e32 v230, 16, v147
	v_and_b32_e32 v231, 0xffff0000, v147
	v_pk_add_f32 v[46:47], v[46:47], v[230:231]
	v_lshlrev_b32_e32 v232, 16, v148
	v_and_b32_e32 v233, 0xffff0000, v148
	v_pk_add_f32 v[48:49], v[48:49], v[232:233]
	v_lshlrev_b32_e32 v234, 16, v149
	v_and_b32_e32 v235, 0xffff0000, v149
	v_pk_add_f32 v[50:51], v[50:51], v[234:235]
	v_lshlrev_b32_e32 v236, 16, v150
	v_and_b32_e32 v237, 0xffff0000, v150
	v_pk_add_f32 v[52:53], v[52:53], v[236:237]
	v_lshlrev_b32_e32 v238, 16, v151
	v_and_b32_e32 v239, 0xffff0000, v151
	v_pk_add_f32 v[54:55], v[54:55], v[238:239]
.Lfin_add_skip_2:
	s_bitcmp1_b32 s36, 3
	s_cbranch_scc0 .Lfin_add_skip_3
	v_lshlrev_b32_e32 v224, 16, v152
	v_and_b32_e32 v225, 0xffff0000, v152
	v_pk_add_f32 v[56:57], v[56:57], v[224:225]
	v_lshlrev_b32_e32 v226, 16, v153
	v_and_b32_e32 v227, 0xffff0000, v153
	v_pk_add_f32 v[58:59], v[58:59], v[226:227]
	v_lshlrev_b32_e32 v228, 16, v154
	v_and_b32_e32 v229, 0xffff0000, v154
	v_pk_add_f32 v[60:61], v[60:61], v[228:229]
	v_lshlrev_b32_e32 v230, 16, v155
	v_and_b32_e32 v231, 0xffff0000, v155
	v_pk_add_f32 v[62:63], v[62:63], v[230:231]
	v_lshlrev_b32_e32 v232, 16, v156
	v_and_b32_e32 v233, 0xffff0000, v156
	v_pk_add_f32 v[64:65], v[64:65], v[232:233]
	v_lshlrev_b32_e32 v234, 16, v157
	v_and_b32_e32 v235, 0xffff0000, v157
	v_pk_add_f32 v[66:67], v[66:67], v[234:235]
	v_lshlrev_b32_e32 v236, 16, v158
	v_and_b32_e32 v237, 0xffff0000, v158
	v_pk_add_f32 v[68:69], v[68:69], v[236:237]
	v_lshlrev_b32_e32 v238, 16, v159
	v_and_b32_e32 v239, 0xffff0000, v159
	v_pk_add_f32 v[70:71], v[70:71], v[238:239]
.Lfin_add_skip_3:
	s_bitcmp1_b32 s36, 4
	s_cbranch_scc0 .Lfin_add_skip_4
	v_lshlrev_b32_e32 v224, 16, v160
	v_and_b32_e32 v225, 0xffff0000, v160
	v_pk_add_f32 v[56:57], v[56:57], v[224:225]
	v_lshlrev_b32_e32 v226, 16, v161
	v_and_b32_e32 v227, 0xffff0000, v161
	v_pk_add_f32 v[58:59], v[58:59], v[226:227]
	v_lshlrev_b32_e32 v228, 16, v162
	v_and_b32_e32 v229, 0xffff0000, v162
	v_pk_add_f32 v[60:61], v[60:61], v[228:229]
	v_lshlrev_b32_e32 v230, 16, v163
	v_and_b32_e32 v231, 0xffff0000, v163
	v_pk_add_f32 v[62:63], v[62:63], v[230:231]
	v_lshlrev_b32_e32 v232, 16, v164
	v_and_b32_e32 v233, 0xffff0000, v164
	v_pk_add_f32 v[64:65], v[64:65], v[232:233]
	v_lshlrev_b32_e32 v234, 16, v165
	v_and_b32_e32 v235, 0xffff0000, v165
	v_pk_add_f32 v[66:67], v[66:67], v[234:235]
	v_lshlrev_b32_e32 v236, 16, v166
	v_and_b32_e32 v237, 0xffff0000, v166
	v_pk_add_f32 v[68:69], v[68:69], v[236:237]
	v_lshlrev_b32_e32 v238, 16, v167
	v_and_b32_e32 v239, 0xffff0000, v167
	v_pk_add_f32 v[70:71], v[70:71], v[238:239]
.Lfin_add_skip_4:
	s_bitcmp1_b32 s36, 5
	s_cbranch_scc0 .Lfin_add_skip_5
	v_lshlrev_b32_e32 v224, 16, v168
	v_and_b32_e32 v225, 0xffff0000, v168
	v_pk_add_f32 v[56:57], v[56:57], v[224:225]
	v_lshlrev_b32_e32 v226, 16, v169
	v_and_b32_e32 v227, 0xffff0000, v169
	v_pk_add_f32 v[58:59], v[58:59], v[226:227]
	v_lshlrev_b32_e32 v228, 16, v170
	v_and_b32_e32 v229, 0xffff0000, v170
	v_pk_add_f32 v[60:61], v[60:61], v[228:229]
	v_lshlrev_b32_e32 v230, 16, v171
	v_and_b32_e32 v231, 0xffff0000, v171
	v_pk_add_f32 v[62:63], v[62:63], v[230:231]
	v_lshlrev_b32_e32 v232, 16, v172
	v_and_b32_e32 v233, 0xffff0000, v172
	v_pk_add_f32 v[64:65], v[64:65], v[232:233]
	v_lshlrev_b32_e32 v234, 16, v173
	v_and_b32_e32 v235, 0xffff0000, v173
	v_pk_add_f32 v[66:67], v[66:67], v[234:235]
	v_lshlrev_b32_e32 v236, 16, v174
	v_and_b32_e32 v237, 0xffff0000, v174
	v_pk_add_f32 v[68:69], v[68:69], v[236:237]
	v_lshlrev_b32_e32 v238, 16, v175
	v_and_b32_e32 v239, 0xffff0000, v175
	v_pk_add_f32 v[70:71], v[70:71], v[238:239]
.Lfin_add_skip_5:
	s_bitcmp1_b32 s36, 6
	s_cbranch_scc0 .Lfin_add_skip_6
	v_lshlrev_b32_e32 v224, 16, v176
	v_and_b32_e32 v225, 0xffff0000, v176
	v_pk_add_f32 v[72:73], v[72:73], v[224:225]
	v_lshlrev_b32_e32 v226, 16, v177
	v_and_b32_e32 v227, 0xffff0000, v177
	v_pk_add_f32 v[74:75], v[74:75], v[226:227]
	v_lshlrev_b32_e32 v228, 16, v178
	v_and_b32_e32 v229, 0xffff0000, v178
	v_pk_add_f32 v[76:77], v[76:77], v[228:229]
	v_lshlrev_b32_e32 v230, 16, v179
	v_and_b32_e32 v231, 0xffff0000, v179
	v_pk_add_f32 v[78:79], v[78:79], v[230:231]
	v_lshlrev_b32_e32 v232, 16, v180
	v_and_b32_e32 v233, 0xffff0000, v180
	v_pk_add_f32 v[80:81], v[80:81], v[232:233]
	v_lshlrev_b32_e32 v234, 16, v181
	v_and_b32_e32 v235, 0xffff0000, v181
	v_pk_add_f32 v[82:83], v[82:83], v[234:235]
	v_lshlrev_b32_e32 v236, 16, v182
	v_and_b32_e32 v237, 0xffff0000, v182
	v_pk_add_f32 v[84:85], v[84:85], v[236:237]
	v_lshlrev_b32_e32 v238, 16, v183
	v_and_b32_e32 v239, 0xffff0000, v183
	v_pk_add_f32 v[86:87], v[86:87], v[238:239]
.Lfin_add_skip_6:
	s_bitcmp1_b32 s36, 7
	s_cbranch_scc0 .Lfin_add_skip_7
	v_lshlrev_b32_e32 v224, 16, v184
	v_and_b32_e32 v225, 0xffff0000, v184
	v_pk_add_f32 v[72:73], v[72:73], v[224:225]
	v_lshlrev_b32_e32 v226, 16, v185
	v_and_b32_e32 v227, 0xffff0000, v185
	v_pk_add_f32 v[74:75], v[74:75], v[226:227]
	v_lshlrev_b32_e32 v228, 16, v186
	v_and_b32_e32 v229, 0xffff0000, v186
	v_pk_add_f32 v[76:77], v[76:77], v[228:229]
	v_lshlrev_b32_e32 v230, 16, v187
	v_and_b32_e32 v231, 0xffff0000, v187
	v_pk_add_f32 v[78:79], v[78:79], v[230:231]
	v_lshlrev_b32_e32 v232, 16, v188
	v_and_b32_e32 v233, 0xffff0000, v188
	v_pk_add_f32 v[80:81], v[80:81], v[232:233]
	v_lshlrev_b32_e32 v234, 16, v189
	v_and_b32_e32 v235, 0xffff0000, v189
	v_pk_add_f32 v[82:83], v[82:83], v[234:235]
	v_lshlrev_b32_e32 v236, 16, v190
	v_and_b32_e32 v237, 0xffff0000, v190
	v_pk_add_f32 v[84:85], v[84:85], v[236:237]
	v_lshlrev_b32_e32 v238, 16, v191
	v_and_b32_e32 v239, 0xffff0000, v191
	v_pk_add_f32 v[86:87], v[86:87], v[238:239]
.Lfin_add_skip_7:
	s_bitcmp1_b32 s36, 8
	s_cbranch_scc0 .Lfin_add_skip_8
	v_lshlrev_b32_e32 v224, 16, v192
	v_and_b32_e32 v225, 0xffff0000, v192
	v_pk_add_f32 v[72:73], v[72:73], v[224:225]
	v_lshlrev_b32_e32 v226, 16, v193
	v_and_b32_e32 v227, 0xffff0000, v193
	v_pk_add_f32 v[74:75], v[74:75], v[226:227]
	v_lshlrev_b32_e32 v228, 16, v194
	v_and_b32_e32 v229, 0xffff0000, v194
	v_pk_add_f32 v[76:77], v[76:77], v[228:229]
	v_lshlrev_b32_e32 v230, 16, v195
	v_and_b32_e32 v231, 0xffff0000, v195
	v_pk_add_f32 v[78:79], v[78:79], v[230:231]
	v_lshlrev_b32_e32 v232, 16, v196
	v_and_b32_e32 v233, 0xffff0000, v196
	v_pk_add_f32 v[80:81], v[80:81], v[232:233]
	v_lshlrev_b32_e32 v234, 16, v197
	v_and_b32_e32 v235, 0xffff0000, v197
	v_pk_add_f32 v[82:83], v[82:83], v[234:235]
	v_lshlrev_b32_e32 v236, 16, v198
	v_and_b32_e32 v237, 0xffff0000, v198
	v_pk_add_f32 v[84:85], v[84:85], v[236:237]
	v_lshlrev_b32_e32 v238, 16, v199
	v_and_b32_e32 v239, 0xffff0000, v199
	v_pk_add_f32 v[86:87], v[86:87], v[238:239]
.Lfin_add_skip_8:
	s_bitcmp1_b32 s36, 9
	s_cbranch_scc0 .Lfin_add_skip_9
	v_lshlrev_b32_e32 v224, 16, v200
	v_and_b32_e32 v225, 0xffff0000, v200
	v_pk_add_f32 v[88:89], v[88:89], v[224:225]
	v_lshlrev_b32_e32 v226, 16, v201
	v_and_b32_e32 v227, 0xffff0000, v201
	v_pk_add_f32 v[90:91], v[90:91], v[226:227]
	v_lshlrev_b32_e32 v228, 16, v202
	v_and_b32_e32 v229, 0xffff0000, v202
	v_pk_add_f32 v[92:93], v[92:93], v[228:229]
	v_lshlrev_b32_e32 v230, 16, v203
	v_and_b32_e32 v231, 0xffff0000, v203
	v_pk_add_f32 v[94:95], v[94:95], v[230:231]
	v_lshlrev_b32_e32 v232, 16, v204
	v_and_b32_e32 v233, 0xffff0000, v204
	v_pk_add_f32 v[96:97], v[96:97], v[232:233]
	v_lshlrev_b32_e32 v234, 16, v205
	v_and_b32_e32 v235, 0xffff0000, v205
	v_pk_add_f32 v[98:99], v[98:99], v[234:235]
	v_lshlrev_b32_e32 v236, 16, v206
	v_and_b32_e32 v237, 0xffff0000, v206
	v_pk_add_f32 v[100:101], v[100:101], v[236:237]
	v_lshlrev_b32_e32 v238, 16, v207
	v_and_b32_e32 v239, 0xffff0000, v207
	v_pk_add_f32 v[102:103], v[102:103], v[238:239]
.Lfin_add_skip_9:
	s_bitcmp1_b32 s36, 10
	s_cbranch_scc0 .Lfin_add_skip_10
	v_lshlrev_b32_e32 v224, 16, v208
	v_and_b32_e32 v225, 0xffff0000, v208
	v_pk_add_f32 v[88:89], v[88:89], v[224:225]
	v_lshlrev_b32_e32 v226, 16, v209
	v_and_b32_e32 v227, 0xffff0000, v209
	v_pk_add_f32 v[90:91], v[90:91], v[226:227]
	v_lshlrev_b32_e32 v228, 16, v210
	v_and_b32_e32 v229, 0xffff0000, v210
	v_pk_add_f32 v[92:93], v[92:93], v[228:229]
	v_lshlrev_b32_e32 v230, 16, v211
	v_and_b32_e32 v231, 0xffff0000, v211
	v_pk_add_f32 v[94:95], v[94:95], v[230:231]
	v_lshlrev_b32_e32 v232, 16, v212
	v_and_b32_e32 v233, 0xffff0000, v212
	v_pk_add_f32 v[96:97], v[96:97], v[232:233]
	v_lshlrev_b32_e32 v234, 16, v213
	v_and_b32_e32 v235, 0xffff0000, v213
	v_pk_add_f32 v[98:99], v[98:99], v[234:235]
	v_lshlrev_b32_e32 v236, 16, v214
	v_and_b32_e32 v237, 0xffff0000, v214
	v_pk_add_f32 v[100:101], v[100:101], v[236:237]
	v_lshlrev_b32_e32 v238, 16, v215
	v_and_b32_e32 v239, 0xffff0000, v215
	v_pk_add_f32 v[102:103], v[102:103], v[238:239]
.Lfin_add_skip_10:
	s_bitcmp1_b32 s36, 11
	s_cbranch_scc0 .Lfin_add_skip_11
	v_lshlrev_b32_e32 v224, 16, v216
	v_and_b32_e32 v225, 0xffff0000, v216
	v_pk_add_f32 v[88:89], v[88:89], v[224:225]
	v_lshlrev_b32_e32 v226, 16, v217
	v_and_b32_e32 v227, 0xffff0000, v217
	v_pk_add_f32 v[90:91], v[90:91], v[226:227]
	v_lshlrev_b32_e32 v228, 16, v218
	v_and_b32_e32 v229, 0xffff0000, v218
	v_pk_add_f32 v[92:93], v[92:93], v[228:229]
	v_lshlrev_b32_e32 v230, 16, v219
	v_and_b32_e32 v231, 0xffff0000, v219
	v_pk_add_f32 v[94:95], v[94:95], v[230:231]
	v_lshlrev_b32_e32 v232, 16, v220
	v_and_b32_e32 v233, 0xffff0000, v220
	v_pk_add_f32 v[96:97], v[96:97], v[232:233]
	v_lshlrev_b32_e32 v234, 16, v221
	v_and_b32_e32 v235, 0xffff0000, v221
	v_pk_add_f32 v[98:99], v[98:99], v[234:235]
	v_lshlrev_b32_e32 v236, 16, v222
	v_and_b32_e32 v237, 0xffff0000, v222
	v_pk_add_f32 v[100:101], v[100:101], v[236:237]
	v_lshlrev_b32_e32 v238, 16, v223
	v_and_b32_e32 v239, 0xffff0000, v223
	v_pk_add_f32 v[102:103], v[102:103], v[238:239]
.Lfin_add_skip_11:
	s_or_b32 s0, s30, s31
	s_or_b32 s0, s0, s40
	s_or_b32 s0, s0, s41
	s_cmp_lg_u32 s0, 0
	s_cbranch_scc1 .Lfin_round
.Lfin_rounds_done:
	v_mul_f32_e32 v234, v41, v41
	v_mul_f32_e32 v235, v43, v43
	v_mul_f32_e32 v236, v45, v45
	v_mul_f32_e32 v237, v47, v47
	v_mul_f32_e32 v238, v49, v49
	v_mul_f32_e32 v239, v51, v51
	v_mul_f32_e32 v240, v53, v53
	v_mul_f32_e32 v241, v55, v55
	v_fmac_f32_e32 v234, v40, v40
	v_fmac_f32_e32 v235, v42, v42
	v_fmac_f32_e32 v236, v44, v44
	v_fmac_f32_e32 v237, v46, v46
	v_fmac_f32_e32 v238, v48, v48
	v_fmac_f32_e32 v239, v50, v50
	v_fmac_f32_e32 v240, v52, v52
	v_fmac_f32_e32 v241, v54, v54
	v_add_f32_e32 v234, v234, v235
	v_add_f32_e32 v236, v236, v237
	v_add_f32_e32 v238, v238, v239
	v_add_f32_e32 v240, v240, v241
	v_add_f32_e32 v224, v236, v234
	v_add_f32_e32 v224, v238, v224
	v_add_f32_e32 v224, v240, v224
	s_lshl_b32 s10, s2, 12
	s_add_u32 s10, s24, s10
	s_addc_u32 s11, s25, 0
	s_nop 1
	v_add_f32_dpp v224, v224, v224 quad_perm:[1,0,3,2] row_mask:0xf bank_mask:0xf bound_ctrl:1
	s_nop 1
	v_add_f32_dpp v224, v224, v224 quad_perm:[2,3,0,1] row_mask:0xf bank_mask:0xf bound_ctrl:1
	s_nop 1
	v_add_f32_dpp v224, v224, v224 row_half_mirror row_mask:0xf bank_mask:0xf bound_ctrl:1
	s_nop 1
	v_add_f32_dpp v224, v224, v224 row_mirror row_mask:0xf bank_mask:0xf bound_ctrl:1
	v_mov_b32_e32 v225, v224
	s_nop 1
	v_permlane16_swap_b32_e32 v224, v225
	v_add_f32_e32 v224, v224, v225
	v_mov_b32_e32 v225, v224
	s_nop 1
	v_permlane32_swap_b32_e32 v224, v225
	v_add_f32_e32 v224, v224, v225
	v_fmamk_f32 v224, v224, 0x3a800000, v108
	v_mul_f32_e32 v225, 0x4f800000, v224
	v_cmp_gt_f32_e32 vcc, s35, v224
	s_nop 1
	v_cndmask_b32_e32 v224, v224, v225, vcc
	v_sqrt_f32_e32 v225, v224
	s_nop 0
	v_add_u32_e32 v226, -1, v225
	v_add_u32_e32 v231, 1, v225
	v_fma_f32 v229, -v226, v225, v224
	v_fma_f32 v230, -v231, v225, v224
	v_cmp_ge_f32_e64 s[12:13], 0, v229
	s_nop 1
	v_cndmask_b32_e64 v225, v225, v226, s[12:13]
	v_cmp_lt_f32_e64 s[12:13], 0, v230
	s_nop 1
	v_cndmask_b32_e64 v225, v225, v231, s[12:13]
	v_mul_f32_e32 v226, 0x37800000, v225
	v_cndmask_b32_e32 v225, v225, v226, vcc
	v_cmp_class_f32_e32 vcc, v224, v109
	s_nop 1
	v_cndmask_b32_e32 v224, v225, v224, vcc
	v_div_scale_f32 v228, s[12:13], v224, v224, 1.0
	v_rcp_f32_e32 v229, v228
	v_div_scale_f32 v230, vcc, 1.0, v224, 1.0
	s_nop 0
	v_fma_f32 v231, -v228, v229, 1.0
	v_fmac_f32_e32 v229, v231, v229
	v_mul_f32_e32 v231, v230, v229
	v_fma_f32 v232, -v228, v231, v230
	v_fmac_f32_e32 v231, v232, v229
	v_fma_f32 v228, -v228, v231, v230
	v_div_fmas_f32 v228, v228, v229, v231
	v_div_fixup_f32 v228, v228, v224, 1.0
	v_pk_mul_f32 v[40:41], v[228:229], v[40:41] op_sel_hi:[0,1]
	v_pk_mul_f32 v[42:43], v[228:229], v[42:43] op_sel_hi:[0,1]
	v_pk_mul_f32 v[44:45], v[228:229], v[44:45] op_sel_hi:[0,1]
	v_pk_mul_f32 v[46:47], v[228:229], v[46:47] op_sel_hi:[0,1]
	v_pk_mul_f32 v[48:49], v[228:229], v[48:49] op_sel_hi:[0,1]
	v_pk_mul_f32 v[50:51], v[228:229], v[50:51] op_sel_hi:[0,1]
	v_pk_mul_f32 v[52:53], v[228:229], v[52:53] op_sel_hi:[0,1]
	v_pk_mul_f32 v[54:55], v[228:229], v[54:55] op_sel_hi:[0,1]
	v_pk_mul_f32 v[40:41], v[112:113], v[40:41]
	v_pk_mul_f32 v[42:43], v[114:115], v[42:43]
	global_store_dwordx4 v107, v[40:43], s[10:11]
	v_pk_mul_f32 v[44:45], v[116:117], v[44:45]
	v_pk_mul_f32 v[46:47], v[118:119], v[46:47]
	global_store_dwordx4 v107, v[44:47], s[10:11] offset:16
	v_pk_mul_f32 v[48:49], v[120:121], v[48:49]
	v_pk_mul_f32 v[50:51], v[122:123], v[50:51]
	global_store_dwordx4 v107, v[48:51], s[10:11] offset:2048
	v_pk_mul_f32 v[52:53], v[124:125], v[52:53]
	v_pk_mul_f32 v[54:55], v[126:127], v[54:55]
	global_store_dwordx4 v107, v[52:55], s[10:11] offset:2064
	s_cmp_eq_u32 s29, 0
	s_cbranch_scc1 .Lfin_skip_rows
	v_mul_f32_e32 v234, v57, v57
	v_mul_f32_e32 v235, v59, v59
	v_mul_f32_e32 v236, v61, v61
	v_mul_f32_e32 v237, v63, v63
	v_mul_f32_e32 v238, v65, v65
	v_mul_f32_e32 v239, v67, v67
	v_mul_f32_e32 v240, v69, v69
	v_mul_f32_e32 v241, v71, v71
	v_fmac_f32_e32 v234, v56, v56
	v_fmac_f32_e32 v235, v58, v58
	v_fmac_f32_e32 v236, v60, v60
	v_fmac_f32_e32 v237, v62, v62
	v_fmac_f32_e32 v238, v64, v64
	v_fmac_f32_e32 v239, v66, v66
	v_fmac_f32_e32 v240, v68, v68
	v_fmac_f32_e32 v241, v70, v70
	v_add_f32_e32 v234, v234, v235
	v_add_f32_e32 v236, v236, v237
	v_add_f32_e32 v238, v238, v239
	v_add_f32_e32 v240, v240, v241
	v_add_f32_e32 v224, v236, v234
	v_add_f32_e32 v224, v238, v224
	v_add_f32_e32 v224, v240, v224
	s_lshl_b32 s10, s3, 12
	s_add_u32 s10, s24, s10
	s_addc_u32 s11, s25, 0
	s_nop 1
	v_add_f32_dpp v224, v224, v224 quad_perm:[1,0,3,2] row_mask:0xf bank_mask:0xf bound_ctrl:1
	s_nop 1
	v_add_f32_dpp v224, v224, v224 quad_perm:[2,3,0,1] row_mask:0xf bank_mask:0xf bound_ctrl:1
	s_nop 1
	v_add_f32_dpp v224, v224, v224 row_half_mirror row_mask:0xf bank_mask:0xf bound_ctrl:1
	s_nop 1
	v_add_f32_dpp v224, v224, v224 row_mirror row_mask:0xf bank_mask:0xf bound_ctrl:1
	v_mov_b32_e32 v225, v224
	s_nop 1
	v_permlane16_swap_b32_e32 v224, v225
	v_add_f32_e32 v224, v224, v225
	v_mov_b32_e32 v225, v224
	s_nop 1
	v_permlane32_swap_b32_e32 v224, v225
	v_add_f32_e32 v224, v224, v225
	v_fmamk_f32 v224, v224, 0x3a800000, v108
	v_mul_f32_e32 v225, 0x4f800000, v224
	v_cmp_gt_f32_e32 vcc, s35, v224
	s_nop 1
	v_cndmask_b32_e32 v224, v224, v225, vcc
	v_sqrt_f32_e32 v225, v224
	s_nop 0
	v_add_u32_e32 v226, -1, v225
	v_add_u32_e32 v231, 1, v225
	v_fma_f32 v229, -v226, v225, v224
	v_fma_f32 v230, -v231, v225, v224
	v_cmp_ge_f32_e64 s[12:13], 0, v229
	s_nop 1
	v_cndmask_b32_e64 v225, v225, v226, s[12:13]
	v_cmp_lt_f32_e64 s[12:13], 0, v230
	s_nop 1
	v_cndmask_b32_e64 v225, v225, v231, s[12:13]
	v_mul_f32_e32 v226, 0x37800000, v225
	v_cndmask_b32_e32 v225, v225, v226, vcc
	v_cmp_class_f32_e32 vcc, v224, v109
	s_nop 1
	v_cndmask_b32_e32 v224, v225, v224, vcc
	v_div_scale_f32 v228, s[12:13], v224, v224, 1.0
	v_rcp_f32_e32 v229, v228
	v_div_scale_f32 v230, vcc, 1.0, v224, 1.0
	s_nop 0
	v_fma_f32 v231, -v228, v229, 1.0
	v_fmac_f32_e32 v229, v231, v229
	v_mul_f32_e32 v231, v230, v229
	v_fma_f32 v232, -v228, v231, v230
	v_fmac_f32_e32 v231, v232, v229
	v_fma_f32 v228, -v228, v231, v230
	v_div_fmas_f32 v228, v228, v229, v231
	v_div_fixup_f32 v228, v228, v224, 1.0
	v_pk_mul_f32 v[56:57], v[228:229], v[56:57] op_sel_hi:[0,1]
	v_pk_mul_f32 v[58:59], v[228:229], v[58:59] op_sel_hi:[0,1]
	v_pk_mul_f32 v[60:61], v[228:229], v[60:61] op_sel_hi:[0,1]
	v_pk_mul_f32 v[62:63], v[228:229], v[62:63] op_sel_hi:[0,1]
	v_pk_mul_f32 v[64:65], v[228:229], v[64:65] op_sel_hi:[0,1]
	v_pk_mul_f32 v[66:67], v[228:229], v[66:67] op_sel_hi:[0,1]
	v_pk_mul_f32 v[68:69], v[228:229], v[68:69] op_sel_hi:[0,1]
	v_pk_mul_f32 v[70:71], v[228:229], v[70:71] op_sel_hi:[0,1]
	v_pk_mul_f32 v[56:57], v[112:113], v[56:57]
	v_pk_mul_f32 v[58:59], v[114:115], v[58:59]
	global_store_dwordx4 v107, v[56:59], s[10:11]
	v_pk_mul_f32 v[60:61], v[116:117], v[60:61]
	v_pk_mul_f32 v[62:63], v[118:119], v[62:63]
	global_store_dwordx4 v107, v[60:63], s[10:11] offset:16
	v_pk_mul_f32 v[64:65], v[120:121], v[64:65]
	v_pk_mul_f32 v[66:67], v[122:123], v[66:67]
	global_store_dwordx4 v107, v[64:67], s[10:11] offset:2048
	v_pk_mul_f32 v[68:69], v[124:125], v[68:69]
	v_pk_mul_f32 v[70:71], v[126:127], v[70:71]
	global_store_dwordx4 v107, v[68:71], s[10:11] offset:2064
	s_cmp_eq_u32 s46, 0
	s_cbranch_scc1 .Lfin_skip_rows
	v_mul_f32_e32 v234, v73, v73
	v_mul_f32_e32 v235, v75, v75
	v_mul_f32_e32 v236, v77, v77
	v_mul_f32_e32 v237, v79, v79
	v_mul_f32_e32 v238, v81, v81
	v_mul_f32_e32 v239, v83, v83
	v_mul_f32_e32 v240, v85, v85
	v_mul_f32_e32 v241, v87, v87
	v_fmac_f32_e32 v234, v72, v72
	v_fmac_f32_e32 v235, v74, v74
	v_fmac_f32_e32 v236, v76, v76
	v_fmac_f32_e32 v237, v78, v78
	v_fmac_f32_e32 v238, v80, v80
	v_fmac_f32_e32 v239, v82, v82
	v_fmac_f32_e32 v240, v84, v84
	v_fmac_f32_e32 v241, v86, v86
	v_add_f32_e32 v234, v234, v235
	v_add_f32_e32 v236, v236, v237
	v_add_f32_e32 v238, v238, v239
	v_add_f32_e32 v240, v240, v241
	v_add_f32_e32 v224, v236, v234
	v_add_f32_e32 v224, v238, v224
	v_add_f32_e32 v224, v240, v224
	s_lshl_b32 s10, s43, 12
	s_add_u32 s10, s24, s10
	s_addc_u32 s11, s25, 0
	s_nop 1
	v_add_f32_dpp v224, v224, v224 quad_perm:[1,0,3,2] row_mask:0xf bank_mask:0xf bound_ctrl:1
	s_nop 1
	v_add_f32_dpp v224, v224, v224 quad_perm:[2,3,0,1] row_mask:0xf bank_mask:0xf bound_ctrl:1
	s_nop 1
	v_add_f32_dpp v224, v224, v224 row_half_mirror row_mask:0xf bank_mask:0xf bound_ctrl:1
	s_nop 1
	v_add_f32_dpp v224, v224, v224 row_mirror row_mask:0xf bank_mask:0xf bound_ctrl:1
	v_mov_b32_e32 v225, v224
	s_nop 1
	v_permlane16_swap_b32_e32 v224, v225
	v_add_f32_e32 v224, v224, v225
	v_mov_b32_e32 v225, v224
	s_nop 1
	v_permlane32_swap_b32_e32 v224, v225
	v_add_f32_e32 v224, v224, v225
	v_fmamk_f32 v224, v224, 0x3a800000, v108
	v_mul_f32_e32 v225, 0x4f800000, v224
	v_cmp_gt_f32_e32 vcc, s35, v224
	s_nop 1
	v_cndmask_b32_e32 v224, v224, v225, vcc
	v_sqrt_f32_e32 v225, v224
	s_nop 0
	v_add_u32_e32 v226, -1, v225
	v_add_u32_e32 v231, 1, v225
	v_fma_f32 v229, -v226, v225, v224
	v_fma_f32 v230, -v231, v225, v224
	v_cmp_ge_f32_e64 s[12:13], 0, v229
	s_nop 1
	v_cndmask_b32_e64 v225, v225, v226, s[12:13]
	v_cmp_lt_f32_e64 s[12:13], 0, v230
	s_nop 1
	v_cndmask_b32_e64 v225, v225, v231, s[12:13]
	v_mul_f32_e32 v226, 0x37800000, v225
	v_cndmask_b32_e32 v225, v225, v226, vcc
	v_cmp_class_f32_e32 vcc, v224, v109
	s_nop 1
	v_cndmask_b32_e32 v224, v225, v224, vcc
	v_div_scale_f32 v228, s[12:13], v224, v224, 1.0
	v_rcp_f32_e32 v229, v228
	v_div_scale_f32 v230, vcc, 1.0, v224, 1.0
	s_nop 0
	v_fma_f32 v231, -v228, v229, 1.0
	v_fmac_f32_e32 v229, v231, v229
	v_mul_f32_e32 v231, v230, v229
	v_fma_f32 v232, -v228, v231, v230
	v_fmac_f32_e32 v231, v232, v229
	v_fma_f32 v228, -v228, v231, v230
	v_div_fmas_f32 v228, v228, v229, v231
	v_div_fixup_f32 v228, v228, v224, 1.0
	v_pk_mul_f32 v[72:73], v[228:229], v[72:73] op_sel_hi:[0,1]
	v_pk_mul_f32 v[74:75], v[228:229], v[74:75] op_sel_hi:[0,1]
	v_pk_mul_f32 v[76:77], v[228:229], v[76:77] op_sel_hi:[0,1]
	v_pk_mul_f32 v[78:79], v[228:229], v[78:79] op_sel_hi:[0,1]
	v_pk_mul_f32 v[80:81], v[228:229], v[80:81] op_sel_hi:[0,1]
	v_pk_mul_f32 v[82:83], v[228:229], v[82:83] op_sel_hi:[0,1]
	v_pk_mul_f32 v[84:85], v[228:229], v[84:85] op_sel_hi:[0,1]
	v_pk_mul_f32 v[86:87], v[228:229], v[86:87] op_sel_hi:[0,1]
	v_pk_mul_f32 v[72:73], v[112:113], v[72:73]
	v_pk_mul_f32 v[74:75], v[114:115], v[74:75]
	global_store_dwordx4 v107, v[72:75], s[10:11]
	v_pk_mul_f32 v[76:77], v[116:117], v[76:77]
	v_pk_mul_f32 v[78:79], v[118:119], v[78:79]
	global_store_dwordx4 v107, v[76:79], s[10:11] offset:16
	v_pk_mul_f32 v[80:81], v[120:121], v[80:81]
	v_pk_mul_f32 v[82:83], v[122:123], v[82:83]
	global_store_dwordx4 v107, v[80:83], s[10:11] offset:2048
	v_pk_mul_f32 v[84:85], v[124:125], v[84:85]
	v_pk_mul_f32 v[86:87], v[126:127], v[86:87]
	global_store_dwordx4 v107, v[84:87], s[10:11] offset:2064
	s_cmp_eq_u32 s47, 0
	s_cbranch_scc1 .Lfin_skip_rows
	v_mul_f32_e32 v234, v89, v89
	v_mul_f32_e32 v235, v91, v91
	v_mul_f32_e32 v236, v93, v93
	v_mul_f32_e32 v237, v95, v95
	v_mul_f32_e32 v238, v97, v97
	v_mul_f32_e32 v239, v99, v99
	v_mul_f32_e32 v240, v101, v101
	v_mul_f32_e32 v241, v103, v103
	v_fmac_f32_e32 v234, v88, v88
	v_fmac_f32_e32 v235, v90, v90
	v_fmac_f32_e32 v236, v92, v92
	v_fmac_f32_e32 v237, v94, v94
	v_fmac_f32_e32 v238, v96, v96
	v_fmac_f32_e32 v239, v98, v98
	v_fmac_f32_e32 v240, v100, v100
	v_fmac_f32_e32 v241, v102, v102
	v_add_f32_e32 v234, v234, v235
	v_add_f32_e32 v236, v236, v237
	v_add_f32_e32 v238, v238, v239
	v_add_f32_e32 v240, v240, v241
	v_add_f32_e32 v224, v236, v234
	v_add_f32_e32 v224, v238, v224
	v_add_f32_e32 v224, v240, v224
	s_lshl_b32 s10, s44, 12
	s_add_u32 s10, s24, s10
	s_addc_u32 s11, s25, 0
	s_nop 1
	v_add_f32_dpp v224, v224, v224 quad_perm:[1,0,3,2] row_mask:0xf bank_mask:0xf bound_ctrl:1
	s_nop 1
	v_add_f32_dpp v224, v224, v224 quad_perm:[2,3,0,1] row_mask:0xf bank_mask:0xf bound_ctrl:1
	s_nop 1
	v_add_f32_dpp v224, v224, v224 row_half_mirror row_mask:0xf bank_mask:0xf bound_ctrl:1
	s_nop 1
	v_add_f32_dpp v224, v224, v224 row_mirror row_mask:0xf bank_mask:0xf bound_ctrl:1
	v_mov_b32_e32 v225, v224
	s_nop 1
	v_permlane16_swap_b32_e32 v224, v225
	v_add_f32_e32 v224, v224, v225
	v_mov_b32_e32 v225, v224
	s_nop 1
	v_permlane32_swap_b32_e32 v224, v225
	v_add_f32_e32 v224, v224, v225
	v_fmamk_f32 v224, v224, 0x3a800000, v108
	v_mul_f32_e32 v225, 0x4f800000, v224
	v_cmp_gt_f32_e32 vcc, s35, v224
	s_nop 1
	v_cndmask_b32_e32 v224, v224, v225, vcc
	v_sqrt_f32_e32 v225, v224
	s_nop 0
	v_add_u32_e32 v226, -1, v225
	v_add_u32_e32 v231, 1, v225
	v_fma_f32 v229, -v226, v225, v224
	v_fma_f32 v230, -v231, v225, v224
	v_cmp_ge_f32_e64 s[12:13], 0, v229
	s_nop 1
	v_cndmask_b32_e64 v225, v225, v226, s[12:13]
	v_cmp_lt_f32_e64 s[12:13], 0, v230
	s_nop 1
	v_cndmask_b32_e64 v225, v225, v231, s[12:13]
	v_mul_f32_e32 v226, 0x37800000, v225
	v_cndmask_b32_e32 v225, v225, v226, vcc
	v_cmp_class_f32_e32 vcc, v224, v109
	s_nop 1
	v_cndmask_b32_e32 v224, v225, v224, vcc
	v_div_scale_f32 v228, s[12:13], v224, v224, 1.0
	v_rcp_f32_e32 v229, v228
	v_div_scale_f32 v230, vcc, 1.0, v224, 1.0
	s_nop 0
	v_fma_f32 v231, -v228, v229, 1.0
	v_fmac_f32_e32 v229, v231, v229
	v_mul_f32_e32 v231, v230, v229
	v_fma_f32 v232, -v228, v231, v230
	v_fmac_f32_e32 v231, v232, v229
	v_fma_f32 v228, -v228, v231, v230
	v_div_fmas_f32 v228, v228, v229, v231
	v_div_fixup_f32 v228, v228, v224, 1.0
	v_pk_mul_f32 v[88:89], v[228:229], v[88:89] op_sel_hi:[0,1]
	v_pk_mul_f32 v[90:91], v[228:229], v[90:91] op_sel_hi:[0,1]
	v_pk_mul_f32 v[92:93], v[228:229], v[92:93] op_sel_hi:[0,1]
	v_pk_mul_f32 v[94:95], v[228:229], v[94:95] op_sel_hi:[0,1]
	v_pk_mul_f32 v[96:97], v[228:229], v[96:97] op_sel_hi:[0,1]
	v_pk_mul_f32 v[98:99], v[228:229], v[98:99] op_sel_hi:[0,1]
	v_pk_mul_f32 v[100:101], v[228:229], v[100:101] op_sel_hi:[0,1]
	v_pk_mul_f32 v[102:103], v[228:229], v[102:103] op_sel_hi:[0,1]
	v_pk_mul_f32 v[88:89], v[112:113], v[88:89]
	v_pk_mul_f32 v[90:91], v[114:115], v[90:91]
	global_store_dwordx4 v107, v[88:91], s[10:11]
	v_pk_mul_f32 v[92:93], v[116:117], v[92:93]
	v_pk_mul_f32 v[94:95], v[118:119], v[94:95]
	global_store_dwordx4 v107, v[92:95], s[10:11] offset:16
	v_pk_mul_f32 v[96:97], v[120:121], v[96:97]
	v_pk_mul_f32 v[98:99], v[122:123], v[98:99]
	global_store_dwordx4 v107, v[96:99], s[10:11] offset:2048
	v_pk_mul_f32 v[100:101], v[124:125], v[100:101]
	v_pk_mul_f32 v[102:103], v[126:127], v[102:103]
	global_store_dwordx4 v107, v[100:103], s[10:11] offset:2064
